# one-time stagger of waves 4-7 at the indexer trip-loop entry (s_sleep) on top of v30
# speedup vs baseline: 1.0294x; 1.0021x over previous
.LBB0_706:
	s_or_b64 exec, exec, s[0:1]
	s_lshl_b32 s2, s16, 2
	s_andn2_b32 s2, s2, 31
	s_and_b32 s0, s16, 7
	s_and_b32 s1, s13, 1
	s_xor_b32 s6, s2, 0x3e0
	s_cmp_eq_u32 s1, 0
	s_cselect_b32 s1, s2, s6
	s_sub_i32 s6, 0x1fe0, s1
	s_lshl_b32 s25, s0, 13
	s_add_i32 s8, s6, s25
	s_lshl_b32 s2, s0, 20
	s_ashr_i32 s9, s8, 31
	s_ashr_i32 s7, s6, 5
	v_readlane_b32 s0, v254, 49
	s_add_u32 s0, s0, s2
	v_readlane_b32 s1, v254, 50
	s_addc_u32 s1, s1, 0
	s_lshl_b64 s[10:11], s[8:9], 5
	v_lshl_add_u64 v[2:3], v[146:147], 0, s[10:11]
	s_waitcnt lgkmcnt(0)
	s_barrier
	global_load_dwordx4 v[66:69], v[2:3], off
	global_load_dwordx4 v[70:73], v[2:3], off offset:16
	s_lshl_b64 s[8:9], s[8:9], 10
	v_lshl_add_u64 v[62:63], v[144:145], 0, s[8:9]
	global_load_dwordx4 v[2:5], v[62:63], off
	global_load_dwordx4 v[6:9], v[62:63], off offset:128
	global_load_dwordx4 v[10:13], v[62:63], off offset:256
	global_load_dwordx4 v[14:17], v[62:63], off offset:384
	global_load_dwordx4 v[18:21], v[62:63], off offset:512
	global_load_dwordx4 v[22:25], v[62:63], off offset:640
	global_load_dwordx4 v[26:29], v[62:63], off offset:768
	global_load_dwordx4 v[30:33], v[62:63], off offset:896
	global_load_dwordx4 v[34:37], v[62:63], off offset:64
	global_load_dwordx4 v[38:41], v[62:63], off offset:192
	global_load_dwordx4 v[42:45], v[62:63], off offset:320
	global_load_dwordx4 v[46:49], v[62:63], off offset:448
	global_load_dwordx4 v[50:53], v[62:63], off offset:576
	global_load_dwordx4 v[54:57], v[62:63], off offset:704
	global_load_dwordx4 v[58:61], v[62:63], off offset:832
	s_nop 0
	global_load_dwordx4 v[62:65], v[62:63], off offset:960
	s_mov_b64 s[10:11], 0x800
	s_add_i32 s7, s7, 1
	s_ashr_i32 s9, s6, 4
	s_lshl_b32 s8, s7, 1
	v_lshl_add_u64 v[172:173], s[0:1], 0, v[154:155]
	s_waitcnt vmcnt(15)
	v_and_b32_e32 v83, 0xffff0000, v3
	v_lshlrev_b32_e32 v82, 16, v3
	s_waitcnt vmcnt(14)
	v_and_b32_e32 v85, 0xffff0000, v7
	v_mul_f32_e32 v156, 0.5, v66
	v_mul_f32_e32 v158, 0.5, v67
	v_and_b32_e32 v67, 0xffff0000, v2
	v_lshlrev_b32_e32 v66, 16, v2
	v_mul_f32_e32 v160, 0.5, v68
	v_mul_f32_e32 v162, 0.5, v69
	v_and_b32_e32 v69, 0xffff0000, v6
	v_lshlrev_b32_e32 v68, 16, v6
	v_lshlrev_b32_e32 v84, 16, v7
	v_pk_fma_f32 v[66:67], v[156:157], v[66:67], 0 op_sel_hi:[0,1,0]
	v_pk_fma_f32 v[82:83], v[156:157], v[82:83], 0 op_sel_hi:[0,1,0]
	v_mul_f32_e32 v164, 0.5, v70
	v_mul_f32_e32 v166, 0.5, v71
	s_waitcnt vmcnt(13)
	v_and_b32_e32 v71, 0xffff0000, v10
	v_lshlrev_b32_e32 v70, 16, v10
	v_and_b32_e32 v87, 0xffff0000, v11
	v_lshlrev_b32_e32 v86, 16, v11
	v_pk_fma_f32 v[66:67], v[158:159], v[68:69], v[66:67] op_sel_hi:[0,1,1]
	v_pk_fma_f32 v[68:69], v[158:159], v[84:85], v[82:83] op_sel_hi:[0,1,1]
	v_mul_f32_e32 v168, 0.5, v72
	v_mul_f32_e32 v170, 0.5, v73
	s_waitcnt vmcnt(12)
	v_and_b32_e32 v73, 0xffff0000, v14
	v_lshlrev_b32_e32 v72, 16, v14
	v_and_b32_e32 v89, 0xffff0000, v15
	v_lshlrev_b32_e32 v88, 16, v15
	v_pk_fma_f32 v[66:67], v[160:161], v[70:71], v[66:67] op_sel_hi:[0,1,1]
	v_pk_fma_f32 v[68:69], v[160:161], v[86:87], v[68:69] op_sel_hi:[0,1,1]
	s_waitcnt vmcnt(11)
	v_and_b32_e32 v75, 0xffff0000, v18
	v_lshlrev_b32_e32 v74, 16, v18
	v_and_b32_e32 v91, 0xffff0000, v19
	v_lshlrev_b32_e32 v90, 16, v19
	v_pk_fma_f32 v[66:67], v[162:163], v[72:73], v[66:67] op_sel_hi:[0,1,1]
	v_pk_fma_f32 v[68:69], v[162:163], v[88:89], v[68:69] op_sel_hi:[0,1,1]
	s_waitcnt vmcnt(10)
	v_and_b32_e32 v77, 0xffff0000, v22
	v_lshlrev_b32_e32 v76, 16, v22
	v_and_b32_e32 v93, 0xffff0000, v23
	v_lshlrev_b32_e32 v92, 16, v23
	v_pk_fma_f32 v[66:67], v[164:165], v[74:75], v[66:67] op_sel_hi:[0,1,1]
	v_pk_fma_f32 v[68:69], v[164:165], v[90:91], v[68:69] op_sel_hi:[0,1,1]
	s_waitcnt vmcnt(9)
	v_and_b32_e32 v79, 0xffff0000, v26
	v_lshlrev_b32_e32 v78, 16, v26
	v_and_b32_e32 v95, 0xffff0000, v27
	v_lshlrev_b32_e32 v94, 16, v27
	v_pk_fma_f32 v[66:67], v[166:167], v[76:77], v[66:67] op_sel_hi:[0,1,1]
	v_pk_fma_f32 v[68:69], v[166:167], v[92:93], v[68:69] op_sel_hi:[0,1,1]
	s_waitcnt vmcnt(8)
	v_and_b32_e32 v81, 0xffff0000, v30
	v_lshlrev_b32_e32 v80, 16, v30
	v_and_b32_e32 v97, 0xffff0000, v31
	v_lshlrev_b32_e32 v96, 16, v31
	v_pk_fma_f32 v[66:67], v[168:169], v[78:79], v[66:67] op_sel_hi:[0,1,1]
	v_pk_fma_f32 v[68:69], v[168:169], v[94:95], v[68:69] op_sel_hi:[0,1,1]
	v_and_b32_e32 v99, 0xffff0000, v4
	v_lshlrev_b32_e32 v98, 16, v4
	v_pk_fma_f32 v[66:67], v[170:171], v[80:81], v[66:67] op_sel_hi:[0,1,1]
	v_pk_fma_f32 v[68:69], v[170:171], v[96:97], v[68:69] op_sel_hi:[0,1,1]
	v_cvt_pk_bf16_f32 v66, v66, v67
	v_cvt_pk_bf16_f32 v67, v68, v69
	v_pk_fma_f32 v[68:69], v[156:157], v[98:99], 0 op_sel_hi:[0,1,0]
	v_and_b32_e32 v71, 0xffff0000, v8
	v_lshlrev_b32_e32 v70, 16, v8
	v_pk_fma_f32 v[68:69], v[158:159], v[70:71], v[68:69] op_sel_hi:[0,1,1]
	v_and_b32_e32 v71, 0xffff0000, v12
	v_lshlrev_b32_e32 v70, 16, v12
	v_pk_fma_f32 v[68:69], v[160:161], v[70:71], v[68:69] op_sel_hi:[0,1,1]
	v_and_b32_e32 v71, 0xffff0000, v16
	v_lshlrev_b32_e32 v70, 16, v16
	v_pk_fma_f32 v[68:69], v[162:163], v[70:71], v[68:69] op_sel_hi:[0,1,1]
	v_and_b32_e32 v71, 0xffff0000, v20
	v_lshlrev_b32_e32 v70, 16, v20
	v_pk_fma_f32 v[68:69], v[164:165], v[70:71], v[68:69] op_sel_hi:[0,1,1]
	v_and_b32_e32 v71, 0xffff0000, v24
	v_lshlrev_b32_e32 v70, 16, v24
	v_pk_fma_f32 v[68:69], v[166:167], v[70:71], v[68:69] op_sel_hi:[0,1,1]
	v_and_b32_e32 v71, 0xffff0000, v28
	v_lshlrev_b32_e32 v70, 16, v28
	v_pk_fma_f32 v[68:69], v[168:169], v[70:71], v[68:69] op_sel_hi:[0,1,1]
	v_and_b32_e32 v71, 0xffff0000, v32
	v_lshlrev_b32_e32 v70, 16, v32
	v_pk_fma_f32 v[68:69], v[170:171], v[70:71], v[68:69] op_sel_hi:[0,1,1]
	v_and_b32_e32 v71, 0xffff0000, v5
	v_lshlrev_b32_e32 v70, 16, v5
	v_pk_fma_f32 v[70:71], v[156:157], v[70:71], 0 op_sel_hi:[0,1,0]
	v_and_b32_e32 v73, 0xffff0000, v9
	v_lshlrev_b32_e32 v72, 16, v9
	v_pk_fma_f32 v[70:71], v[158:159], v[72:73], v[70:71] op_sel_hi:[0,1,1]
	v_and_b32_e32 v73, 0xffff0000, v13
	v_lshlrev_b32_e32 v72, 16, v13
	v_pk_fma_f32 v[70:71], v[160:161], v[72:73], v[70:71] op_sel_hi:[0,1,1]
	v_and_b32_e32 v73, 0xffff0000, v17
	v_lshlrev_b32_e32 v72, 16, v17
	v_pk_fma_f32 v[70:71], v[162:163], v[72:73], v[70:71] op_sel_hi:[0,1,1]
	v_and_b32_e32 v73, 0xffff0000, v21
	v_lshlrev_b32_e32 v72, 16, v21
	v_pk_fma_f32 v[70:71], v[164:165], v[72:73], v[70:71] op_sel_hi:[0,1,1]
	v_and_b32_e32 v73, 0xffff0000, v25
	v_lshlrev_b32_e32 v72, 16, v25
	v_pk_fma_f32 v[70:71], v[166:167], v[72:73], v[70:71] op_sel_hi:[0,1,1]
	v_and_b32_e32 v73, 0xffff0000, v29
	v_lshlrev_b32_e32 v72, 16, v29
	v_pk_fma_f32 v[70:71], v[168:169], v[72:73], v[70:71] op_sel_hi:[0,1,1]
	v_and_b32_e32 v73, 0xffff0000, v33
	v_lshlrev_b32_e32 v72, 16, v33
	v_pk_fma_f32 v[70:71], v[170:171], v[72:73], v[70:71] op_sel_hi:[0,1,1]
	v_cvt_pk_bf16_f32 v68, v68, v69
	v_cvt_pk_bf16_f32 v69, v70, v71
	s_waitcnt vmcnt(7)
	v_and_b32_e32 v71, 0xffff0000, v34
	v_lshlrev_b32_e32 v70, 16, v34
	v_pk_fma_f32 v[70:71], v[156:157], v[70:71], 0 op_sel_hi:[0,1,0]
	s_waitcnt vmcnt(6)
	v_and_b32_e32 v73, 0xffff0000, v38
	v_lshlrev_b32_e32 v72, 16, v38
	v_pk_fma_f32 v[70:71], v[158:159], v[72:73], v[70:71] op_sel_hi:[0,1,1]
	s_waitcnt vmcnt(5)
	v_and_b32_e32 v73, 0xffff0000, v42
	v_lshlrev_b32_e32 v72, 16, v42
	v_pk_fma_f32 v[70:71], v[160:161], v[72:73], v[70:71] op_sel_hi:[0,1,1]
	s_waitcnt vmcnt(4)
	v_and_b32_e32 v73, 0xffff0000, v46
	v_lshlrev_b32_e32 v72, 16, v46
	v_pk_fma_f32 v[70:71], v[162:163], v[72:73], v[70:71] op_sel_hi:[0,1,1]
	s_waitcnt vmcnt(3)
	v_and_b32_e32 v73, 0xffff0000, v50
	v_lshlrev_b32_e32 v72, 16, v50
	v_pk_fma_f32 v[70:71], v[164:165], v[72:73], v[70:71] op_sel_hi:[0,1,1]
	s_waitcnt vmcnt(2)
	v_and_b32_e32 v73, 0xffff0000, v54
	v_lshlrev_b32_e32 v72, 16, v54
	v_pk_fma_f32 v[70:71], v[166:167], v[72:73], v[70:71] op_sel_hi:[0,1,1]
	s_waitcnt vmcnt(1)
	v_and_b32_e32 v73, 0xffff0000, v58
	v_lshlrev_b32_e32 v72, 16, v58
	v_pk_fma_f32 v[70:71], v[168:169], v[72:73], v[70:71] op_sel_hi:[0,1,1]
	s_waitcnt vmcnt(0)
	v_and_b32_e32 v73, 0xffff0000, v62
	v_lshlrev_b32_e32 v72, 16, v62
	v_pk_fma_f32 v[70:71], v[170:171], v[72:73], v[70:71] op_sel_hi:[0,1,1]
	v_and_b32_e32 v73, 0xffff0000, v35
	v_lshlrev_b32_e32 v72, 16, v35
	v_pk_fma_f32 v[72:73], v[156:157], v[72:73], 0 op_sel_hi:[0,1,0]
	v_and_b32_e32 v75, 0xffff0000, v39
	v_lshlrev_b32_e32 v74, 16, v39
	v_pk_fma_f32 v[72:73], v[158:159], v[74:75], v[72:73] op_sel_hi:[0,1,1]
	v_and_b32_e32 v75, 0xffff0000, v43
	v_lshlrev_b32_e32 v74, 16, v43
	v_pk_fma_f32 v[72:73], v[160:161], v[74:75], v[72:73] op_sel_hi:[0,1,1]
	v_and_b32_e32 v75, 0xffff0000, v47
	v_lshlrev_b32_e32 v74, 16, v47
	v_pk_fma_f32 v[72:73], v[162:163], v[74:75], v[72:73] op_sel_hi:[0,1,1]
	v_and_b32_e32 v75, 0xffff0000, v51
	v_lshlrev_b32_e32 v74, 16, v51
	v_pk_fma_f32 v[72:73], v[164:165], v[74:75], v[72:73] op_sel_hi:[0,1,1]
	v_and_b32_e32 v75, 0xffff0000, v55
	v_lshlrev_b32_e32 v74, 16, v55
	v_pk_fma_f32 v[72:73], v[166:167], v[74:75], v[72:73] op_sel_hi:[0,1,1]
	v_and_b32_e32 v75, 0xffff0000, v59
	v_lshlrev_b32_e32 v74, 16, v59
	v_pk_fma_f32 v[72:73], v[168:169], v[74:75], v[72:73] op_sel_hi:[0,1,1]
	v_and_b32_e32 v75, 0xffff0000, v63
	v_lshlrev_b32_e32 v74, 16, v63
	v_pk_fma_f32 v[72:73], v[170:171], v[74:75], v[72:73] op_sel_hi:[0,1,1]
	v_cvt_pk_bf16_f32 v70, v70, v71
	v_cvt_pk_bf16_f32 v71, v72, v73
	v_and_b32_e32 v73, 0xffff0000, v36
	v_lshlrev_b32_e32 v72, 16, v36
	v_pk_fma_f32 v[72:73], v[156:157], v[72:73], 0 op_sel_hi:[0,1,0]
	v_and_b32_e32 v75, 0xffff0000, v40
	v_lshlrev_b32_e32 v74, 16, v40
	v_pk_fma_f32 v[72:73], v[158:159], v[74:75], v[72:73] op_sel_hi:[0,1,1]
	v_and_b32_e32 v75, 0xffff0000, v44
	v_lshlrev_b32_e32 v74, 16, v44
	v_pk_fma_f32 v[72:73], v[160:161], v[74:75], v[72:73] op_sel_hi:[0,1,1]
	v_and_b32_e32 v75, 0xffff0000, v48
	v_lshlrev_b32_e32 v74, 16, v48
	v_pk_fma_f32 v[72:73], v[162:163], v[74:75], v[72:73] op_sel_hi:[0,1,1]
	v_and_b32_e32 v75, 0xffff0000, v52
	v_lshlrev_b32_e32 v74, 16, v52
	v_pk_fma_f32 v[72:73], v[164:165], v[74:75], v[72:73] op_sel_hi:[0,1,1]
	v_and_b32_e32 v75, 0xffff0000, v56
	v_lshlrev_b32_e32 v74, 16, v56
	v_pk_fma_f32 v[72:73], v[166:167], v[74:75], v[72:73] op_sel_hi:[0,1,1]
	v_and_b32_e32 v75, 0xffff0000, v60
	v_lshlrev_b32_e32 v74, 16, v60
	v_pk_fma_f32 v[72:73], v[168:169], v[74:75], v[72:73] op_sel_hi:[0,1,1]
	v_and_b32_e32 v75, 0xffff0000, v64
	v_lshlrev_b32_e32 v74, 16, v64
	v_pk_fma_f32 v[72:73], v[170:171], v[74:75], v[72:73] op_sel_hi:[0,1,1]
	v_and_b32_e32 v75, 0xffff0000, v37
	v_lshlrev_b32_e32 v74, 16, v37
	v_pk_fma_f32 v[74:75], v[156:157], v[74:75], 0 op_sel_hi:[0,1,0]
	v_and_b32_e32 v77, 0xffff0000, v41
	v_lshlrev_b32_e32 v76, 16, v41
	v_pk_fma_f32 v[74:75], v[158:159], v[76:77], v[74:75] op_sel_hi:[0,1,1]
	v_and_b32_e32 v77, 0xffff0000, v45
	v_lshlrev_b32_e32 v76, 16, v45
	v_pk_fma_f32 v[74:75], v[160:161], v[76:77], v[74:75] op_sel_hi:[0,1,1]
	v_and_b32_e32 v77, 0xffff0000, v49
	v_lshlrev_b32_e32 v76, 16, v49
	v_pk_fma_f32 v[74:75], v[162:163], v[76:77], v[74:75] op_sel_hi:[0,1,1]
	v_and_b32_e32 v77, 0xffff0000, v53
	v_lshlrev_b32_e32 v76, 16, v53
	v_pk_fma_f32 v[74:75], v[164:165], v[76:77], v[74:75] op_sel_hi:[0,1,1]
	v_and_b32_e32 v77, 0xffff0000, v57
	v_lshlrev_b32_e32 v76, 16, v57
	v_pk_fma_f32 v[74:75], v[166:167], v[76:77], v[74:75] op_sel_hi:[0,1,1]
	v_and_b32_e32 v77, 0xffff0000, v61
	v_lshlrev_b32_e32 v76, 16, v61
	v_pk_fma_f32 v[74:75], v[168:169], v[76:77], v[74:75] op_sel_hi:[0,1,1]
	v_and_b32_e32 v77, 0xffff0000, v65
	v_lshlrev_b32_e32 v76, 16, v65
	v_pk_fma_f32 v[74:75], v[170:171], v[76:77], v[74:75] op_sel_hi:[0,1,1]
	v_cvt_pk_bf16_f32 v72, v72, v73
	v_cvt_pk_bf16_f32 v73, v74, v75
	v_lshl_add_u64 v[74:75], s[0:1], 0, v[152:153]
	v_lshl_add_u64 v[74:75], v[74:75], 0, v[154:155]
	global_load_dwordx4 v[134:137], v[74:75], off
	global_load_dwordx4 v[130:133], v[74:75], off offset:1024
	v_lshl_add_u64 v[76:77], v[74:75], 0, s[10:11]
	global_load_dwordx4 v[126:129], v[76:77], off
	global_load_dwordx4 v[122:125], v[76:77], off offset:1024
	s_mov_b64 s[10:11], 0x1000
	v_lshl_add_u64 v[76:77], v[74:75], 0, s[10:11]
	global_load_dwordx4 v[110:113], v[76:77], off
	global_load_dwordx4 v[106:109], v[76:77], off offset:1024
	s_mov_b64 s[10:11], 0x1800
	v_lshl_add_u64 v[74:75], v[74:75], 0, s[10:11]
	global_load_dwordx4 v[94:97], v[74:75], off
	global_load_dwordx4 v[90:93], v[74:75], off offset:1024
	v_readlane_b32 s10, v254, 53
	s_waitcnt vmcnt(0)
	s_add_i32 s9, s10, s9
	s_min_i32 s9, s8, s9
	s_cmp_ge_i32 s12, s9
	s_cbranch_scc1 .LBB0_709
	v_readfirstlane_b32 s0, v138
	s_nop 3
	s_cmp_lt_u32 s0, 16
	s_cbranch_scc1 .Lstagger_skip
	s_sleep 55
.Lstagger_skip:
	v_mov_b32_e32 v157, v205
	v_mov_b64_e32 v[174:175], v[148:149]
	s_mov_b32 s52, s12
